# layer-1 PEER table rows converted by idle workgroups during layer-0 gemm2/3/4 last rounds, 3 slots, throttled (one s_sleep 127 per row)
# speedup vs baseline: 1.0009x; 1.0009x over previous
.LBB0_611:
	v_readlane_b32 s4, v255, 36
	v_readlane_b32 s8, v252, 0
	s_add_i32 s5, s4, 7
	v_readlane_b32 s9, v252, 1
	s_cmp_ge_i32 s5, s9
	v_readlane_b32 s10, v252, 2
	v_readlane_b32 s11, v252, 3
	s_cbranch_scc1 .LBB0_661
	v_readlane_b32 s4, v255, 34
	s_nop 0
	s_cmp_lg_u32 s4, 0
	s_cbranch_scc1 .Ldfa_done
	s_cmp_gt_u32 s82, 32
	s_cselect_b32 s11, 32, 0
	s_cmp_lt_u32 s2, s11
	s_cbranch_scc1 .Ldfa_done
	s_sub_u32 s10, s82, s11
	s_lshl_b32 s10, s10, 3
	s_sub_u32 s4, s2, s11
	s_lshl_b32 s4, s4, 3
	v_readfirstlane_b32 s11, v0
	s_lshr_b32 s11, s11, 6
	s_add_u32 s4, s4, s11
	s_add_u32 s4, s4, 0x4000
	s_cmp_ge_u32 s4, 0x76b0
	s_cbranch_scc1 .Ldfa_done
	v_readlane_b32 s6, v252, 4
	v_readlane_b32 s7, v252, 5
	s_nop 0
	s_sub_u32 s6, s6, 0x38
	s_subb_u32 s7, s7, 0
	s_load_dwordx2 s[8:9], s[6:7], 0x0
	s_load_dwordx2 s[6:7], s[6:7], 0x20
	v_and_b32_e32 v6, 63, v0
	v_lshlrev_b32_e32 v7, 4, v6
	v_lshrrev_b32_e32 v56, 5, v6
	v_and_b32_e32 v57, 31, v6
	v_lshlrev_b32_e32 v56, 21, v56
	v_lshl_add_u32 v56, v57, 2, v56
	v_add_u32_e32 v56, 0xaa00000, v56
	s_mov_b64 exec, -1
	s_waitcnt lgkmcnt(0)
	s_lshl_b32 s11, s4, 13
	v_add_u32_e32 v40, s11, v7
	v_add_u32_e32 v41, 0x1000, v40
	global_load_dwordx4 v[8:11], v40, s[8:9] nt
	global_load_dwordx4 v[12:15], v40, s[8:9] offset:1024 nt
	global_load_dwordx4 v[16:19], v40, s[8:9] offset:2048 nt
	global_load_dwordx4 v[20:23], v40, s[8:9] offset:3072 nt
	global_load_dwordx4 v[24:27], v41, s[8:9] nt
	global_load_dwordx4 v[28:31], v41, s[8:9] offset:1024 nt
	global_load_dwordx4 v[32:35], v41, s[8:9] offset:2048 nt
	global_load_dwordx4 v[36:39], v41, s[8:9] offset:3072 nt
.Ldfa_loop:
	s_add_u32 s11, s4, s10
	s_min_u32 s11, s11, 0x76af
	s_mov_b32 s101, s11
	s_lshl_b32 s11, s101, 13
	v_add_u32_e32 v40, s11, v7
	v_add_u32_e32 v41, 0x1000, v40
	global_load_dwordx4 v[76:79], v40, s[8:9] nt
	global_load_dwordx4 v[80:83], v40, s[8:9] offset:1024 nt
	global_load_dwordx4 v[84:87], v40, s[8:9] offset:2048 nt
	global_load_dwordx4 v[88:91], v40, s[8:9] offset:3072 nt
	global_load_dwordx4 v[92:95], v41, s[8:9] nt
	global_load_dwordx4 v[96:99], v41, s[8:9] offset:1024 nt
	global_load_dwordx4 v[100:103], v41, s[8:9] offset:2048 nt
	global_load_dwordx4 v[104:107], v41, s[8:9] offset:3072 nt
	s_waitcnt vmcnt(8)
	v_max3_f32 v42, |v8|, |v9|, |v10|
	v_max3_f32 v43, |v12|, |v13|, |v14|
	v_max3_f32 v44, |v16|, |v17|, |v18|
	v_max3_f32 v45, |v20|, |v21|, |v22|
	v_max3_f32 v46, |v24|, |v25|, |v26|
	v_max3_f32 v47, |v28|, |v29|, |v30|
	v_max3_f32 v48, |v32|, |v33|, |v34|
	v_max3_f32 v49, |v36|, |v37|, |v38|
	v_max_f32_e64 v42, v42, |v11|
	v_max_f32_e64 v43, v43, |v15|
	v_max_f32_e64 v44, v44, |v19|
	v_max_f32_e64 v45, v45, |v23|
	v_max_f32_e64 v46, v46, |v27|
	v_max_f32_e64 v47, v47, |v31|
	v_max_f32_e64 v48, v48, |v35|
	v_max_f32_e64 v49, v49, |v39|
	v_max3_f32 v42, v42, v43, v44
	v_max3_f32 v45, v45, v46, v47
	v_max3_f32 v42, v42, v45, v48
	v_max_f32_e32 v42, v42, v49
	s_nop 1
	v_max_f32_dpp v43, v42, v42 quad_perm:[1,0,3,2] row_mask:0xf bank_mask:0xf bound_ctrl:1
	s_nop 1
	v_max_f32_dpp v42, v43, v43 quad_perm:[2,3,0,1] row_mask:0xf bank_mask:0xf bound_ctrl:1
	s_nop 1
	v_max_f32_dpp v43, v42, v42 row_half_mirror row_mask:0xf bank_mask:0xf bound_ctrl:1
	s_nop 1
	v_max_f32_dpp v42, v43, v43 row_mirror row_mask:0xf bank_mask:0xf bound_ctrl:1
	s_nop 1
	v_mov_b32_e32 v43, v42
	s_nop 1
	v_permlane16_swap_b32_e32 v42, v43
	v_max_f32_e32 v42, v42, v43
	v_mov_b32_e32 v43, v42
	s_nop 1
	v_permlane32_swap_b32_e32 v42, v43
	v_max_f32_e32 v49, v42, v43
	v_mul_f32_e32 v44, 0x3b124925, v49
	s_lshl_b32 s11, s4, 2
	s_add_u32 s11, s11, 0x12a00000
	v_mov_b32_e32 v45, s11
	s_mov_b64 exec, 1
	global_store_dword v45, v44, s[6:7]
	s_mov_b64 exec, -1
	v_mov_b32_e32 v46, 0x43e00000
	v_div_scale_f32 v42, s[100:101], v49, v49, v46
	v_rcp_f32_e32 v43, v42
	s_nop 0
	v_fma_f32 v44, -v42, v43, 1.0
	v_fmac_f32_e32 v43, v44, v43
	v_div_scale_f32 v44, vcc, v46, v49, v46
	v_mul_f32_e32 v45, v44, v43
	v_fma_f32 v47, -v42, v45, v44
	v_fmac_f32_e32 v45, v47, v43
	v_fma_f32 v42, -v42, v45, v44
	s_nop 1
	v_div_fmas_f32 v42, v42, v43, v45
	v_div_fixup_f32 v42, v42, v49, v46
	v_cmp_lt_f32_e32 vcc, 0, v49
	s_nop 1
	v_cndmask_b32_e32 v48, 0, v42, vcc
	v_mul_f32_e32 v8, v8, v48
	v_mul_f32_e32 v9, v9, v48
	v_mul_f32_e32 v10, v10, v48
	v_mul_f32_e32 v11, v11, v48
	v_mul_f32_e32 v12, v12, v48
	v_mul_f32_e32 v13, v13, v48
	v_mul_f32_e32 v14, v14, v48
	v_mul_f32_e32 v15, v15, v48
	v_mul_f32_e32 v16, v16, v48
	v_mul_f32_e32 v17, v17, v48
	v_mul_f32_e32 v18, v18, v48
	v_mul_f32_e32 v19, v19, v48
	v_mul_f32_e32 v20, v20, v48
	v_mul_f32_e32 v21, v21, v48
	v_mul_f32_e32 v22, v22, v48
	v_mul_f32_e32 v23, v23, v48
	v_mul_f32_e32 v24, v24, v48
	v_mul_f32_e32 v25, v25, v48
	v_mul_f32_e32 v26, v26, v48
	v_mul_f32_e32 v27, v27, v48
	v_mul_f32_e32 v28, v28, v48
	v_mul_f32_e32 v29, v29, v48
	v_mul_f32_e32 v30, v30, v48
	v_mul_f32_e32 v31, v31, v48
	v_mul_f32_e32 v32, v32, v48
	v_mul_f32_e32 v33, v33, v48
	v_mul_f32_e32 v34, v34, v48
	v_mul_f32_e32 v35, v35, v48
	v_mul_f32_e32 v36, v36, v48
	v_mul_f32_e32 v37, v37, v48
	v_mul_f32_e32 v38, v38, v48
	v_mul_f32_e32 v39, v39, v48
	v_mov_b32_e32 v58, 0
	v_mov_b32_e32 v59, 0
	v_mov_b32_e32 v60, 0
	v_mov_b32_e32 v61, 0
	v_mov_b32_e32 v62, 0
	v_mov_b32_e32 v63, 0
	v_mov_b32_e32 v64, 0
	v_mov_b32_e32 v65, 0
	v_cvt_pk_fp8_f32 v58, v8, v9
	v_cvt_pk_fp8_f32 v59, v12, v13
	v_cvt_pk_fp8_f32 v60, v16, v17
	v_cvt_pk_fp8_f32 v61, v20, v21
	v_cvt_pk_fp8_f32 v62, v24, v25
	v_cvt_pk_fp8_f32 v63, v28, v29
	v_cvt_pk_fp8_f32 v64, v32, v33
	v_cvt_pk_fp8_f32 v65, v36, v37
	v_cvt_pk_fp8_f32 v58, v10, v11 op_sel:[0,0,1]
	v_cvt_pk_fp8_f32 v59, v14, v15 op_sel:[0,0,1]
	v_cvt_pk_fp8_f32 v60, v18, v19 op_sel:[0,0,1]
	v_cvt_pk_fp8_f32 v61, v22, v23 op_sel:[0,0,1]
	v_cvt_pk_fp8_f32 v62, v26, v27 op_sel:[0,0,1]
	v_cvt_pk_fp8_f32 v63, v30, v31 op_sel:[0,0,1]
	v_cvt_pk_fp8_f32 v64, v34, v35 op_sel:[0,0,1]
	v_cvt_pk_fp8_f32 v65, v38, v39 op_sel:[0,0,1]
	s_and_b32 s11, s4, 0x3fff
	s_lshl_b32 s11, s11, 7
	s_lshr_b32 s101, s4, 14
	s_lshl_b32 s101, s101, 25
	s_add_u32 s11, s11, s101
	v_add_u32_e32 v66, s11, v56
	v_add_u32_e32 v67, 0x400000, v66
	v_add_u32_e32 v68, 0x800000, v66
	v_add_u32_e32 v69, 0xc00000, v66
	v_add_u32_e32 v70, 0x1000000, v66
	v_add_u32_e32 v71, 0x1400000, v66
	v_add_u32_e32 v72, 0x1800000, v66
	v_add_u32_e32 v73, 0x1c00000, v66
	global_store_dword v66, v58, s[6:7] nt
	global_store_dword v67, v59, s[6:7] nt
	global_store_dword v68, v60, s[6:7] nt
	global_store_dword v69, v61, s[6:7] nt
	global_store_dword v70, v62, s[6:7] nt
	global_store_dword v71, v63, s[6:7] nt
	global_store_dword v72, v64, s[6:7] nt
	global_store_dword v73, v65, s[6:7] nt
	s_sleep 127
	s_add_u32 s4, s4, s10
	s_cmp_ge_u32 s4, 0x76b0
	s_cbranch_scc1 .Ldfa_done
	s_add_u32 s11, s4, s10
	s_min_u32 s11, s11, 0x76af
	s_mov_b32 s101, s11
	s_lshl_b32 s11, s101, 13
	v_add_u32_e32 v40, s11, v7
	v_add_u32_e32 v41, 0x1000, v40
	global_load_dwordx4 v[8:11], v40, s[8:9] nt
	global_load_dwordx4 v[12:15], v40, s[8:9] offset:1024 nt
	global_load_dwordx4 v[16:19], v40, s[8:9] offset:2048 nt
	global_load_dwordx4 v[20:23], v40, s[8:9] offset:3072 nt
	global_load_dwordx4 v[24:27], v41, s[8:9] nt
	global_load_dwordx4 v[28:31], v41, s[8:9] offset:1024 nt
	global_load_dwordx4 v[32:35], v41, s[8:9] offset:2048 nt
	global_load_dwordx4 v[36:39], v41, s[8:9] offset:3072 nt
	s_waitcnt vmcnt(8)
	v_max3_f32 v42, |v76|, |v77|, |v78|
	v_max3_f32 v43, |v80|, |v81|, |v82|
	v_max3_f32 v44, |v84|, |v85|, |v86|
	v_max3_f32 v45, |v88|, |v89|, |v90|
	v_max3_f32 v46, |v92|, |v93|, |v94|
	v_max3_f32 v47, |v96|, |v97|, |v98|
	v_max3_f32 v48, |v100|, |v101|, |v102|
	v_max3_f32 v49, |v104|, |v105|, |v106|
	v_max_f32_e64 v42, v42, |v79|
	v_max_f32_e64 v43, v43, |v83|
	v_max_f32_e64 v44, v44, |v87|
	v_max_f32_e64 v45, v45, |v91|
	v_max_f32_e64 v46, v46, |v95|
	v_max_f32_e64 v47, v47, |v99|
	v_max_f32_e64 v48, v48, |v103|
	v_max_f32_e64 v49, v49, |v107|
	v_max3_f32 v42, v42, v43, v44
	v_max3_f32 v45, v45, v46, v47
	v_max3_f32 v42, v42, v45, v48
	v_max_f32_e32 v42, v42, v49
	s_nop 1
	v_max_f32_dpp v43, v42, v42 quad_perm:[1,0,3,2] row_mask:0xf bank_mask:0xf bound_ctrl:1
	s_nop 1
	v_max_f32_dpp v42, v43, v43 quad_perm:[2,3,0,1] row_mask:0xf bank_mask:0xf bound_ctrl:1
	s_nop 1
	v_max_f32_dpp v43, v42, v42 row_half_mirror row_mask:0xf bank_mask:0xf bound_ctrl:1
	s_nop 1
	v_max_f32_dpp v42, v43, v43 row_mirror row_mask:0xf bank_mask:0xf bound_ctrl:1
	s_nop 1
	v_mov_b32_e32 v43, v42
	s_nop 1
	v_permlane16_swap_b32_e32 v42, v43
	v_max_f32_e32 v42, v42, v43
	v_mov_b32_e32 v43, v42
	s_nop 1
	v_permlane32_swap_b32_e32 v42, v43
	v_max_f32_e32 v49, v42, v43
	v_mul_f32_e32 v44, 0x3b124925, v49
	s_lshl_b32 s11, s4, 2
	s_add_u32 s11, s11, 0x12a00000
	v_mov_b32_e32 v45, s11
	s_mov_b64 exec, 1
	global_store_dword v45, v44, s[6:7]
	s_mov_b64 exec, -1
	v_mov_b32_e32 v46, 0x43e00000
	v_div_scale_f32 v42, s[100:101], v49, v49, v46
	v_rcp_f32_e32 v43, v42
	s_nop 0
	v_fma_f32 v44, -v42, v43, 1.0
	v_fmac_f32_e32 v43, v44, v43
	v_div_scale_f32 v44, vcc, v46, v49, v46
	v_mul_f32_e32 v45, v44, v43
	v_fma_f32 v47, -v42, v45, v44
	v_fmac_f32_e32 v45, v47, v43
	v_fma_f32 v42, -v42, v45, v44
	s_nop 1
	v_div_fmas_f32 v42, v42, v43, v45
	v_div_fixup_f32 v42, v42, v49, v46
	v_cmp_lt_f32_e32 vcc, 0, v49
	s_nop 1
	v_cndmask_b32_e32 v48, 0, v42, vcc
	v_mul_f32_e32 v76, v76, v48
	v_mul_f32_e32 v77, v77, v48
	v_mul_f32_e32 v78, v78, v48
	v_mul_f32_e32 v79, v79, v48
	v_mul_f32_e32 v80, v80, v48
	v_mul_f32_e32 v81, v81, v48
	v_mul_f32_e32 v82, v82, v48
	v_mul_f32_e32 v83, v83, v48
	v_mul_f32_e32 v84, v84, v48
	v_mul_f32_e32 v85, v85, v48
	v_mul_f32_e32 v86, v86, v48
	v_mul_f32_e32 v87, v87, v48
	v_mul_f32_e32 v88, v88, v48
	v_mul_f32_e32 v89, v89, v48
	v_mul_f32_e32 v90, v90, v48
	v_mul_f32_e32 v91, v91, v48
	v_mul_f32_e32 v92, v92, v48
	v_mul_f32_e32 v93, v93, v48
	v_mul_f32_e32 v94, v94, v48
	v_mul_f32_e32 v95, v95, v48
	v_mul_f32_e32 v96, v96, v48
	v_mul_f32_e32 v97, v97, v48
	v_mul_f32_e32 v98, v98, v48
	v_mul_f32_e32 v99, v99, v48
	v_mul_f32_e32 v100, v100, v48
	v_mul_f32_e32 v101, v101, v48
	v_mul_f32_e32 v102, v102, v48
	v_mul_f32_e32 v103, v103, v48
	v_mul_f32_e32 v104, v104, v48
	v_mul_f32_e32 v105, v105, v48
	v_mul_f32_e32 v106, v106, v48
	v_mul_f32_e32 v107, v107, v48
	v_mov_b32_e32 v58, 0
	v_mov_b32_e32 v59, 0
	v_mov_b32_e32 v60, 0
	v_mov_b32_e32 v61, 0
	v_mov_b32_e32 v62, 0
	v_mov_b32_e32 v63, 0
	v_mov_b32_e32 v64, 0
	v_mov_b32_e32 v65, 0
	v_cvt_pk_fp8_f32 v58, v76, v77
	v_cvt_pk_fp8_f32 v59, v80, v81
	v_cvt_pk_fp8_f32 v60, v84, v85
	v_cvt_pk_fp8_f32 v61, v88, v89
	v_cvt_pk_fp8_f32 v62, v92, v93
	v_cvt_pk_fp8_f32 v63, v96, v97
	v_cvt_pk_fp8_f32 v64, v100, v101
	v_cvt_pk_fp8_f32 v65, v104, v105
	v_cvt_pk_fp8_f32 v58, v78, v79 op_sel:[0,0,1]
	v_cvt_pk_fp8_f32 v59, v82, v83 op_sel:[0,0,1]
	v_cvt_pk_fp8_f32 v60, v86, v87 op_sel:[0,0,1]
	v_cvt_pk_fp8_f32 v61, v90, v91 op_sel:[0,0,1]
	v_cvt_pk_fp8_f32 v62, v94, v95 op_sel:[0,0,1]
	v_cvt_pk_fp8_f32 v63, v98, v99 op_sel:[0,0,1]
	v_cvt_pk_fp8_f32 v64, v102, v103 op_sel:[0,0,1]
	v_cvt_pk_fp8_f32 v65, v106, v107 op_sel:[0,0,1]
	s_and_b32 s11, s4, 0x3fff
	s_lshl_b32 s11, s11, 7
	s_lshr_b32 s101, s4, 14
	s_lshl_b32 s101, s101, 25
	s_add_u32 s11, s11, s101
	v_add_u32_e32 v66, s11, v56
	v_add_u32_e32 v67, 0x400000, v66
	v_add_u32_e32 v68, 0x800000, v66
	v_add_u32_e32 v69, 0xc00000, v66
	v_add_u32_e32 v70, 0x1000000, v66
	v_add_u32_e32 v71, 0x1400000, v66
	v_add_u32_e32 v72, 0x1800000, v66
	v_add_u32_e32 v73, 0x1c00000, v66
	global_store_dword v66, v58, s[6:7] nt
	global_store_dword v67, v59, s[6:7] nt
	global_store_dword v68, v60, s[6:7] nt
	global_store_dword v69, v61, s[6:7] nt
	global_store_dword v70, v62, s[6:7] nt
	global_store_dword v71, v63, s[6:7] nt
	global_store_dword v72, v64, s[6:7] nt
	global_store_dword v73, v65, s[6:7] nt
	s_sleep 127
	s_add_u32 s4, s4, s10
	s_cmp_ge_u32 s4, 0x76b0
	s_cbranch_scc1 .Ldfa_done
	s_branch .Ldfa_loop

.LBB0_709:
	v_readlane_b32 s4, v255, 36
	v_readlane_b32 s8, v252, 0
	s_add_i32 s5, s4, 8
	v_readlane_b32 s9, v252, 1
	s_cmp_ge_i32 s5, s9
	v_readlane_b32 s10, v252, 2
	v_readlane_b32 s11, v252, 3
	s_cbranch_scc1 .LBB0_721
	v_readlane_b32 s4, v255, 34
	s_nop 0
	s_cmp_lg_u32 s4, 0
	s_cbranch_scc1 .Ldfb1_done
	s_cmp_gt_u32 s82, 32
	s_cselect_b32 s11, 32, 0
	s_cmp_lt_u32 s2, s11
	s_cbranch_scc1 .Ldfb1_done
	s_sub_u32 s10, s82, s11
	s_lshl_b32 s10, s10, 3
	s_sub_u32 s4, s2, s11
	s_lshl_b32 s4, s4, 3
	v_readfirstlane_b32 s11, v0
	s_lshr_b32 s11, s11, 6
	s_add_u32 s4, s4, s11
	s_add_u32 s4, s4, 0x76b0
	s_cmp_ge_u32 s4, 0x8000
	s_cbranch_scc1 .Ldfb1_done
	v_readlane_b32 s6, v252, 4
	v_readlane_b32 s7, v252, 5
	s_nop 0
	s_sub_u32 s6, s6, 0x38
	s_subb_u32 s7, s7, 0
	s_load_dwordx2 s[8:9], s[6:7], 0x0
	s_load_dwordx2 s[6:7], s[6:7], 0x20
	v_and_b32_e32 v6, 63, v0
	v_lshlrev_b32_e32 v7, 4, v6
	v_lshrrev_b32_e32 v56, 5, v6
	v_and_b32_e32 v57, 31, v6
	v_lshlrev_b32_e32 v56, 21, v56
	v_lshl_add_u32 v56, v57, 2, v56
	v_add_u32_e32 v56, 0xaa00000, v56
	s_mov_b64 exec, -1
	s_waitcnt lgkmcnt(0)
	s_lshl_b32 s11, s4, 13
	v_add_u32_e32 v40, s11, v7
	v_add_u32_e32 v41, 0x1000, v40
	global_load_dwordx4 v[8:11], v40, s[8:9] nt
	global_load_dwordx4 v[12:15], v40, s[8:9] offset:1024 nt
	global_load_dwordx4 v[16:19], v40, s[8:9] offset:2048 nt
	global_load_dwordx4 v[20:23], v40, s[8:9] offset:3072 nt
	global_load_dwordx4 v[24:27], v41, s[8:9] nt
	global_load_dwordx4 v[28:31], v41, s[8:9] offset:1024 nt
	global_load_dwordx4 v[32:35], v41, s[8:9] offset:2048 nt
	global_load_dwordx4 v[36:39], v41, s[8:9] offset:3072 nt
.Ldfb1_loop:
	s_add_u32 s11, s4, s10
	s_min_u32 s11, s11, 0x7fff
	s_mov_b32 s101, s11
	s_lshl_b32 s11, s101, 13
	v_add_u32_e32 v40, s11, v7
	v_add_u32_e32 v41, 0x1000, v40
	global_load_dwordx4 v[76:79], v40, s[8:9] nt
	global_load_dwordx4 v[80:83], v40, s[8:9] offset:1024 nt
	global_load_dwordx4 v[84:87], v40, s[8:9] offset:2048 nt
	global_load_dwordx4 v[88:91], v40, s[8:9] offset:3072 nt
	global_load_dwordx4 v[92:95], v41, s[8:9] nt
	global_load_dwordx4 v[96:99], v41, s[8:9] offset:1024 nt
	global_load_dwordx4 v[100:103], v41, s[8:9] offset:2048 nt
	global_load_dwordx4 v[104:107], v41, s[8:9] offset:3072 nt
	s_waitcnt vmcnt(8)
	v_max3_f32 v42, |v8|, |v9|, |v10|
	v_max3_f32 v43, |v12|, |v13|, |v14|
	v_max3_f32 v44, |v16|, |v17|, |v18|
	v_max3_f32 v45, |v20|, |v21|, |v22|
	v_max3_f32 v46, |v24|, |v25|, |v26|
	v_max3_f32 v47, |v28|, |v29|, |v30|
	v_max3_f32 v48, |v32|, |v33|, |v34|
	v_max3_f32 v49, |v36|, |v37|, |v38|
	v_max_f32_e64 v42, v42, |v11|
	v_max_f32_e64 v43, v43, |v15|
	v_max_f32_e64 v44, v44, |v19|
	v_max_f32_e64 v45, v45, |v23|
	v_max_f32_e64 v46, v46, |v27|
	v_max_f32_e64 v47, v47, |v31|
	v_max_f32_e64 v48, v48, |v35|
	v_max_f32_e64 v49, v49, |v39|
	v_max3_f32 v42, v42, v43, v44
	v_max3_f32 v45, v45, v46, v47
	v_max3_f32 v42, v42, v45, v48
	v_max_f32_e32 v42, v42, v49
	s_nop 1
	v_max_f32_dpp v43, v42, v42 quad_perm:[1,0,3,2] row_mask:0xf bank_mask:0xf bound_ctrl:1
	s_nop 1
	v_max_f32_dpp v42, v43, v43 quad_perm:[2,3,0,1] row_mask:0xf bank_mask:0xf bound_ctrl:1
	s_nop 1
	v_max_f32_dpp v43, v42, v42 row_half_mirror row_mask:0xf bank_mask:0xf bound_ctrl:1
	s_nop 1
	v_max_f32_dpp v42, v43, v43 row_mirror row_mask:0xf bank_mask:0xf bound_ctrl:1
	s_nop 1
	v_mov_b32_e32 v43, v42
	s_nop 1
	v_permlane16_swap_b32_e32 v42, v43
	v_max_f32_e32 v42, v42, v43
	v_mov_b32_e32 v43, v42
	s_nop 1
	v_permlane32_swap_b32_e32 v42, v43
	v_max_f32_e32 v49, v42, v43
	v_mul_f32_e32 v44, 0x3b124925, v49
	s_lshl_b32 s11, s4, 2
	s_add_u32 s11, s11, 0x12a00000
	v_mov_b32_e32 v45, s11
	s_mov_b64 exec, 1
	global_store_dword v45, v44, s[6:7]
	s_mov_b64 exec, -1
	v_mov_b32_e32 v46, 0x43e00000
	v_div_scale_f32 v42, s[100:101], v49, v49, v46
	v_rcp_f32_e32 v43, v42
	s_nop 0
	v_fma_f32 v44, -v42, v43, 1.0
	v_fmac_f32_e32 v43, v44, v43
	v_div_scale_f32 v44, vcc, v46, v49, v46
	v_mul_f32_e32 v45, v44, v43
	v_fma_f32 v47, -v42, v45, v44
	v_fmac_f32_e32 v45, v47, v43
	v_fma_f32 v42, -v42, v45, v44
	s_nop 1
	v_div_fmas_f32 v42, v42, v43, v45
	v_div_fixup_f32 v42, v42, v49, v46
	v_cmp_lt_f32_e32 vcc, 0, v49
	s_nop 1
	v_cndmask_b32_e32 v48, 0, v42, vcc
	v_mul_f32_e32 v8, v8, v48
	v_mul_f32_e32 v9, v9, v48
	v_mul_f32_e32 v10, v10, v48
	v_mul_f32_e32 v11, v11, v48
	v_mul_f32_e32 v12, v12, v48
	v_mul_f32_e32 v13, v13, v48
	v_mul_f32_e32 v14, v14, v48
	v_mul_f32_e32 v15, v15, v48
	v_mul_f32_e32 v16, v16, v48
	v_mul_f32_e32 v17, v17, v48
	v_mul_f32_e32 v18, v18, v48
	v_mul_f32_e32 v19, v19, v48
	v_mul_f32_e32 v20, v20, v48
	v_mul_f32_e32 v21, v21, v48
	v_mul_f32_e32 v22, v22, v48
	v_mul_f32_e32 v23, v23, v48
	v_mul_f32_e32 v24, v24, v48
	v_mul_f32_e32 v25, v25, v48
	v_mul_f32_e32 v26, v26, v48
	v_mul_f32_e32 v27, v27, v48
	v_mul_f32_e32 v28, v28, v48
	v_mul_f32_e32 v29, v29, v48
	v_mul_f32_e32 v30, v30, v48
	v_mul_f32_e32 v31, v31, v48
	v_mul_f32_e32 v32, v32, v48
	v_mul_f32_e32 v33, v33, v48
	v_mul_f32_e32 v34, v34, v48
	v_mul_f32_e32 v35, v35, v48
	v_mul_f32_e32 v36, v36, v48
	v_mul_f32_e32 v37, v37, v48
	v_mul_f32_e32 v38, v38, v48
	v_mul_f32_e32 v39, v39, v48
	v_mov_b32_e32 v58, 0
	v_mov_b32_e32 v59, 0
	v_mov_b32_e32 v60, 0
	v_mov_b32_e32 v61, 0
	v_mov_b32_e32 v62, 0
	v_mov_b32_e32 v63, 0
	v_mov_b32_e32 v64, 0
	v_mov_b32_e32 v65, 0
	v_cvt_pk_fp8_f32 v58, v8, v9
	v_cvt_pk_fp8_f32 v59, v12, v13
	v_cvt_pk_fp8_f32 v60, v16, v17
	v_cvt_pk_fp8_f32 v61, v20, v21
	v_cvt_pk_fp8_f32 v62, v24, v25
	v_cvt_pk_fp8_f32 v63, v28, v29
	v_cvt_pk_fp8_f32 v64, v32, v33
	v_cvt_pk_fp8_f32 v65, v36, v37
	v_cvt_pk_fp8_f32 v58, v10, v11 op_sel:[0,0,1]
	v_cvt_pk_fp8_f32 v59, v14, v15 op_sel:[0,0,1]
	v_cvt_pk_fp8_f32 v60, v18, v19 op_sel:[0,0,1]
	v_cvt_pk_fp8_f32 v61, v22, v23 op_sel:[0,0,1]
	v_cvt_pk_fp8_f32 v62, v26, v27 op_sel:[0,0,1]
	v_cvt_pk_fp8_f32 v63, v30, v31 op_sel:[0,0,1]
	v_cvt_pk_fp8_f32 v64, v34, v35 op_sel:[0,0,1]
	v_cvt_pk_fp8_f32 v65, v38, v39 op_sel:[0,0,1]
	s_and_b32 s11, s4, 0x3fff
	s_lshl_b32 s11, s11, 7
	s_lshr_b32 s101, s4, 14
	s_lshl_b32 s101, s101, 25
	s_add_u32 s11, s11, s101
	v_add_u32_e32 v66, s11, v56
	v_add_u32_e32 v67, 0x400000, v66
	v_add_u32_e32 v68, 0x800000, v66
	v_add_u32_e32 v69, 0xc00000, v66
	v_add_u32_e32 v70, 0x1000000, v66
	v_add_u32_e32 v71, 0x1400000, v66
	v_add_u32_e32 v72, 0x1800000, v66
	v_add_u32_e32 v73, 0x1c00000, v66
	global_store_dword v66, v58, s[6:7] nt
	global_store_dword v67, v59, s[6:7] nt
	global_store_dword v68, v60, s[6:7] nt
	global_store_dword v69, v61, s[6:7] nt
	global_store_dword v70, v62, s[6:7] nt
	global_store_dword v71, v63, s[6:7] nt
	global_store_dword v72, v64, s[6:7] nt
	global_store_dword v73, v65, s[6:7] nt
	s_sleep 127
	s_add_u32 s4, s4, s10
	s_cmp_ge_u32 s4, 0x8000
	s_cbranch_scc1 .Ldfb1_done
	s_add_u32 s11, s4, s10
	s_min_u32 s11, s11, 0x7fff
	s_mov_b32 s101, s11
	s_lshl_b32 s11, s101, 13
	v_add_u32_e32 v40, s11, v7
	v_add_u32_e32 v41, 0x1000, v40
	global_load_dwordx4 v[8:11], v40, s[8:9] nt
	global_load_dwordx4 v[12:15], v40, s[8:9] offset:1024 nt
	global_load_dwordx4 v[16:19], v40, s[8:9] offset:2048 nt
	global_load_dwordx4 v[20:23], v40, s[8:9] offset:3072 nt
	global_load_dwordx4 v[24:27], v41, s[8:9] nt
	global_load_dwordx4 v[28:31], v41, s[8:9] offset:1024 nt
	global_load_dwordx4 v[32:35], v41, s[8:9] offset:2048 nt
	global_load_dwordx4 v[36:39], v41, s[8:9] offset:3072 nt
	s_waitcnt vmcnt(8)
	v_max3_f32 v42, |v76|, |v77|, |v78|
	v_max3_f32 v43, |v80|, |v81|, |v82|
	v_max3_f32 v44, |v84|, |v85|, |v86|
	v_max3_f32 v45, |v88|, |v89|, |v90|
	v_max3_f32 v46, |v92|, |v93|, |v94|
	v_max3_f32 v47, |v96|, |v97|, |v98|
	v_max3_f32 v48, |v100|, |v101|, |v102|
	v_max3_f32 v49, |v104|, |v105|, |v106|
	v_max_f32_e64 v42, v42, |v79|
	v_max_f32_e64 v43, v43, |v83|
	v_max_f32_e64 v44, v44, |v87|
	v_max_f32_e64 v45, v45, |v91|
	v_max_f32_e64 v46, v46, |v95|
	v_max_f32_e64 v47, v47, |v99|
	v_max_f32_e64 v48, v48, |v103|
	v_max_f32_e64 v49, v49, |v107|
	v_max3_f32 v42, v42, v43, v44
	v_max3_f32 v45, v45, v46, v47
	v_max3_f32 v42, v42, v45, v48
	v_max_f32_e32 v42, v42, v49
	s_nop 1
	v_max_f32_dpp v43, v42, v42 quad_perm:[1,0,3,2] row_mask:0xf bank_mask:0xf bound_ctrl:1
	s_nop 1
	v_max_f32_dpp v42, v43, v43 quad_perm:[2,3,0,1] row_mask:0xf bank_mask:0xf bound_ctrl:1
	s_nop 1
	v_max_f32_dpp v43, v42, v42 row_half_mirror row_mask:0xf bank_mask:0xf bound_ctrl:1
	s_nop 1
	v_max_f32_dpp v42, v43, v43 row_mirror row_mask:0xf bank_mask:0xf bound_ctrl:1
	s_nop 1
	v_mov_b32_e32 v43, v42
	s_nop 1
	v_permlane16_swap_b32_e32 v42, v43
	v_max_f32_e32 v42, v42, v43
	v_mov_b32_e32 v43, v42
	s_nop 1
	v_permlane32_swap_b32_e32 v42, v43
	v_max_f32_e32 v49, v42, v43
	v_mul_f32_e32 v44, 0x3b124925, v49
	s_lshl_b32 s11, s4, 2
	s_add_u32 s11, s11, 0x12a00000
	v_mov_b32_e32 v45, s11
	s_mov_b64 exec, 1
	global_store_dword v45, v44, s[6:7]
	s_mov_b64 exec, -1
	v_mov_b32_e32 v46, 0x43e00000
	v_div_scale_f32 v42, s[100:101], v49, v49, v46
	v_rcp_f32_e32 v43, v42
	s_nop 0
	v_fma_f32 v44, -v42, v43, 1.0
	v_fmac_f32_e32 v43, v44, v43
	v_div_scale_f32 v44, vcc, v46, v49, v46
	v_mul_f32_e32 v45, v44, v43
	v_fma_f32 v47, -v42, v45, v44
	v_fmac_f32_e32 v45, v47, v43
	v_fma_f32 v42, -v42, v45, v44
	s_nop 1
	v_div_fmas_f32 v42, v42, v43, v45
	v_div_fixup_f32 v42, v42, v49, v46
	v_cmp_lt_f32_e32 vcc, 0, v49
	s_nop 1
	v_cndmask_b32_e32 v48, 0, v42, vcc
	v_mul_f32_e32 v76, v76, v48
	v_mul_f32_e32 v77, v77, v48
	v_mul_f32_e32 v78, v78, v48
	v_mul_f32_e32 v79, v79, v48
	v_mul_f32_e32 v80, v80, v48
	v_mul_f32_e32 v81, v81, v48
	v_mul_f32_e32 v82, v82, v48
	v_mul_f32_e32 v83, v83, v48
	v_mul_f32_e32 v84, v84, v48
	v_mul_f32_e32 v85, v85, v48
	v_mul_f32_e32 v86, v86, v48
	v_mul_f32_e32 v87, v87, v48
	v_mul_f32_e32 v88, v88, v48
	v_mul_f32_e32 v89, v89, v48
	v_mul_f32_e32 v90, v90, v48
	v_mul_f32_e32 v91, v91, v48
	v_mul_f32_e32 v92, v92, v48
	v_mul_f32_e32 v93, v93, v48
	v_mul_f32_e32 v94, v94, v48
	v_mul_f32_e32 v95, v95, v48
	v_mul_f32_e32 v96, v96, v48
	v_mul_f32_e32 v97, v97, v48
	v_mul_f32_e32 v98, v98, v48
	v_mul_f32_e32 v99, v99, v48
	v_mul_f32_e32 v100, v100, v48
	v_mul_f32_e32 v101, v101, v48
	v_mul_f32_e32 v102, v102, v48
	v_mul_f32_e32 v103, v103, v48
	v_mul_f32_e32 v104, v104, v48
	v_mul_f32_e32 v105, v105, v48
	v_mul_f32_e32 v106, v106, v48
	v_mul_f32_e32 v107, v107, v48
	v_mov_b32_e32 v58, 0
	v_mov_b32_e32 v59, 0
	v_mov_b32_e32 v60, 0
	v_mov_b32_e32 v61, 0
	v_mov_b32_e32 v62, 0
	v_mov_b32_e32 v63, 0
	v_mov_b32_e32 v64, 0
	v_mov_b32_e32 v65, 0
	v_cvt_pk_fp8_f32 v58, v76, v77
	v_cvt_pk_fp8_f32 v59, v80, v81
	v_cvt_pk_fp8_f32 v60, v84, v85
	v_cvt_pk_fp8_f32 v61, v88, v89
	v_cvt_pk_fp8_f32 v62, v92, v93
	v_cvt_pk_fp8_f32 v63, v96, v97
	v_cvt_pk_fp8_f32 v64, v100, v101
	v_cvt_pk_fp8_f32 v65, v104, v105
	v_cvt_pk_fp8_f32 v58, v78, v79 op_sel:[0,0,1]
	v_cvt_pk_fp8_f32 v59, v82, v83 op_sel:[0,0,1]
	v_cvt_pk_fp8_f32 v60, v86, v87 op_sel:[0,0,1]
	v_cvt_pk_fp8_f32 v61, v90, v91 op_sel:[0,0,1]
	v_cvt_pk_fp8_f32 v62, v94, v95 op_sel:[0,0,1]
	v_cvt_pk_fp8_f32 v63, v98, v99 op_sel:[0,0,1]
	v_cvt_pk_fp8_f32 v64, v102, v103 op_sel:[0,0,1]
	v_cvt_pk_fp8_f32 v65, v106, v107 op_sel:[0,0,1]
	s_and_b32 s11, s4, 0x3fff
	s_lshl_b32 s11, s11, 7
	s_lshr_b32 s101, s4, 14
	s_lshl_b32 s101, s101, 25
	s_add_u32 s11, s11, s101
	v_add_u32_e32 v66, s11, v56
	v_add_u32_e32 v67, 0x400000, v66
	v_add_u32_e32 v68, 0x800000, v66
	v_add_u32_e32 v69, 0xc00000, v66
	v_add_u32_e32 v70, 0x1000000, v66
	v_add_u32_e32 v71, 0x1400000, v66
	v_add_u32_e32 v72, 0x1800000, v66
	v_add_u32_e32 v73, 0x1c00000, v66
	global_store_dword v66, v58, s[6:7] nt
	global_store_dword v67, v59, s[6:7] nt
	global_store_dword v68, v60, s[6:7] nt
	global_store_dword v69, v61, s[6:7] nt
	global_store_dword v70, v62, s[6:7] nt
	global_store_dword v71, v63, s[6:7] nt
	global_store_dword v72, v64, s[6:7] nt
	global_store_dword v73, v65, s[6:7] nt
	s_sleep 127
	s_add_u32 s4, s4, s10
	s_cmp_ge_u32 s4, 0x8000
	s_cbranch_scc1 .Ldfb1_done
	s_branch .Ldfb1_loop

.Ldfb1_end:
	v_readlane_b32 s4, v255, 36
	v_readlane_b32 s4, v255, 34
	s_nop 0
	s_cmp_lg_u32 s4, 0
	s_cbranch_scc1 .Ldfb2_done
	s_cmp_gt_u32 s82, 32
	s_cselect_b32 s11, 32, 0
	s_cmp_lt_u32 s2, s11
	s_cbranch_scc1 .Ldfb2_done
	s_sub_u32 s10, s82, s11
	s_lshl_b32 s10, s10, 3
	s_sub_u32 s4, s2, s11
	s_lshl_b32 s4, s4, 3
	v_readfirstlane_b32 s11, v0
	s_lshr_b32 s11, s11, 6
	s_add_u32 s4, s4, s11
	s_add_u32 s4, s4, 0x4000
	s_cmp_ge_u32 s4, 0x59d8
	s_cbranch_scc1 .Ldfb2_done
	v_readlane_b32 s6, v252, 4
	v_readlane_b32 s7, v252, 5
	s_nop 0
	s_sub_u32 s6, s6, 0x38
	s_subb_u32 s7, s7, 0
	s_load_dwordx2 s[8:9], s[6:7], 0x8
	s_load_dwordx2 s[6:7], s[6:7], 0x20
	v_and_b32_e32 v6, 63, v0
	v_lshlrev_b32_e32 v7, 4, v6
	v_lshrrev_b32_e32 v56, 5, v6
	v_and_b32_e32 v57, 31, v6
	v_lshlrev_b32_e32 v56, 21, v56
	v_lshl_add_u32 v56, v57, 2, v56
	v_add_u32_e32 v56, 0xea00000, v56
	s_mov_b64 exec, -1
	s_waitcnt lgkmcnt(0)
	s_lshl_b32 s11, s4, 13
	v_add_u32_e32 v40, s11, v7
	v_add_u32_e32 v41, 0x1000, v40
	global_load_dwordx4 v[8:11], v40, s[8:9] nt
	global_load_dwordx4 v[12:15], v40, s[8:9] offset:1024 nt
	global_load_dwordx4 v[16:19], v40, s[8:9] offset:2048 nt
	global_load_dwordx4 v[20:23], v40, s[8:9] offset:3072 nt
	global_load_dwordx4 v[24:27], v41, s[8:9] nt
	global_load_dwordx4 v[28:31], v41, s[8:9] offset:1024 nt
	global_load_dwordx4 v[32:35], v41, s[8:9] offset:2048 nt
	global_load_dwordx4 v[36:39], v41, s[8:9] offset:3072 nt
.Ldfb2_loop:
	s_add_u32 s11, s4, s10
	s_min_u32 s11, s11, 0x59d7
	s_mov_b32 s101, s11
	s_lshl_b32 s11, s101, 13
	v_add_u32_e32 v40, s11, v7
	v_add_u32_e32 v41, 0x1000, v40
	global_load_dwordx4 v[76:79], v40, s[8:9] nt
	global_load_dwordx4 v[80:83], v40, s[8:9] offset:1024 nt
	global_load_dwordx4 v[84:87], v40, s[8:9] offset:2048 nt
	global_load_dwordx4 v[88:91], v40, s[8:9] offset:3072 nt
	global_load_dwordx4 v[92:95], v41, s[8:9] nt
	global_load_dwordx4 v[96:99], v41, s[8:9] offset:1024 nt
	global_load_dwordx4 v[100:103], v41, s[8:9] offset:2048 nt
	global_load_dwordx4 v[104:107], v41, s[8:9] offset:3072 nt
	s_waitcnt vmcnt(8)
	v_max3_f32 v42, |v8|, |v9|, |v10|
	v_max3_f32 v43, |v12|, |v13|, |v14|
	v_max3_f32 v44, |v16|, |v17|, |v18|
	v_max3_f32 v45, |v20|, |v21|, |v22|
	v_max3_f32 v46, |v24|, |v25|, |v26|
	v_max3_f32 v47, |v28|, |v29|, |v30|
	v_max3_f32 v48, |v32|, |v33|, |v34|
	v_max3_f32 v49, |v36|, |v37|, |v38|
	v_max_f32_e64 v42, v42, |v11|
	v_max_f32_e64 v43, v43, |v15|
	v_max_f32_e64 v44, v44, |v19|
	v_max_f32_e64 v45, v45, |v23|
	v_max_f32_e64 v46, v46, |v27|
	v_max_f32_e64 v47, v47, |v31|
	v_max_f32_e64 v48, v48, |v35|
	v_max_f32_e64 v49, v49, |v39|
	v_max3_f32 v42, v42, v43, v44
	v_max3_f32 v45, v45, v46, v47
	v_max3_f32 v42, v42, v45, v48
	v_max_f32_e32 v42, v42, v49
	s_nop 1
	v_max_f32_dpp v43, v42, v42 quad_perm:[1,0,3,2] row_mask:0xf bank_mask:0xf bound_ctrl:1
	s_nop 1
	v_max_f32_dpp v42, v43, v43 quad_perm:[2,3,0,1] row_mask:0xf bank_mask:0xf bound_ctrl:1
	s_nop 1
	v_max_f32_dpp v43, v42, v42 row_half_mirror row_mask:0xf bank_mask:0xf bound_ctrl:1
	s_nop 1
	v_max_f32_dpp v42, v43, v43 row_mirror row_mask:0xf bank_mask:0xf bound_ctrl:1
	s_nop 1
	v_mov_b32_e32 v43, v42
	s_nop 1
	v_permlane16_swap_b32_e32 v42, v43
	v_max_f32_e32 v42, v42, v43
	v_mov_b32_e32 v43, v42
	s_nop 1
	v_permlane32_swap_b32_e32 v42, v43
	v_max_f32_e32 v49, v42, v43
	v_mul_f32_e32 v44, 0x3b124925, v49
	s_lshl_b32 s11, s4, 2
	s_add_u32 s11, s11, 0x12a20000
	v_mov_b32_e32 v45, s11
	s_mov_b64 exec, 1
	global_store_dword v45, v44, s[6:7]
	s_mov_b64 exec, -1
	v_mov_b32_e32 v46, 0x43e00000
	v_div_scale_f32 v42, s[100:101], v49, v49, v46
	v_rcp_f32_e32 v43, v42
	s_nop 0
	v_fma_f32 v44, -v42, v43, 1.0
	v_fmac_f32_e32 v43, v44, v43
	v_div_scale_f32 v44, vcc, v46, v49, v46
	v_mul_f32_e32 v45, v44, v43
	v_fma_f32 v47, -v42, v45, v44
	v_fmac_f32_e32 v45, v47, v43
	v_fma_f32 v42, -v42, v45, v44
	s_nop 1
	v_div_fmas_f32 v42, v42, v43, v45
	v_div_fixup_f32 v42, v42, v49, v46
	v_cmp_lt_f32_e32 vcc, 0, v49
	s_nop 1
	v_cndmask_b32_e32 v48, 0, v42, vcc
	v_mul_f32_e32 v8, v8, v48
	v_mul_f32_e32 v9, v9, v48
	v_mul_f32_e32 v10, v10, v48
	v_mul_f32_e32 v11, v11, v48
	v_mul_f32_e32 v12, v12, v48
	v_mul_f32_e32 v13, v13, v48
	v_mul_f32_e32 v14, v14, v48
	v_mul_f32_e32 v15, v15, v48
	v_mul_f32_e32 v16, v16, v48
	v_mul_f32_e32 v17, v17, v48
	v_mul_f32_e32 v18, v18, v48
	v_mul_f32_e32 v19, v19, v48
	v_mul_f32_e32 v20, v20, v48
	v_mul_f32_e32 v21, v21, v48
	v_mul_f32_e32 v22, v22, v48
	v_mul_f32_e32 v23, v23, v48
	v_mul_f32_e32 v24, v24, v48
	v_mul_f32_e32 v25, v25, v48
	v_mul_f32_e32 v26, v26, v48
	v_mul_f32_e32 v27, v27, v48
	v_mul_f32_e32 v28, v28, v48
	v_mul_f32_e32 v29, v29, v48
	v_mul_f32_e32 v30, v30, v48
	v_mul_f32_e32 v31, v31, v48
	v_mul_f32_e32 v32, v32, v48
	v_mul_f32_e32 v33, v33, v48
	v_mul_f32_e32 v34, v34, v48
	v_mul_f32_e32 v35, v35, v48
	v_mul_f32_e32 v36, v36, v48
	v_mul_f32_e32 v37, v37, v48
	v_mul_f32_e32 v38, v38, v48
	v_mul_f32_e32 v39, v39, v48
	v_mov_b32_e32 v58, 0
	v_mov_b32_e32 v59, 0
	v_mov_b32_e32 v60, 0
	v_mov_b32_e32 v61, 0
	v_mov_b32_e32 v62, 0
	v_mov_b32_e32 v63, 0
	v_mov_b32_e32 v64, 0
	v_mov_b32_e32 v65, 0
	v_cvt_pk_fp8_f32 v58, v8, v9
	v_cvt_pk_fp8_f32 v59, v12, v13
	v_cvt_pk_fp8_f32 v60, v16, v17
	v_cvt_pk_fp8_f32 v61, v20, v21
	v_cvt_pk_fp8_f32 v62, v24, v25
	v_cvt_pk_fp8_f32 v63, v28, v29
	v_cvt_pk_fp8_f32 v64, v32, v33
	v_cvt_pk_fp8_f32 v65, v36, v37
	v_cvt_pk_fp8_f32 v58, v10, v11 op_sel:[0,0,1]
	v_cvt_pk_fp8_f32 v59, v14, v15 op_sel:[0,0,1]
	v_cvt_pk_fp8_f32 v60, v18, v19 op_sel:[0,0,1]
	v_cvt_pk_fp8_f32 v61, v22, v23 op_sel:[0,0,1]
	v_cvt_pk_fp8_f32 v62, v26, v27 op_sel:[0,0,1]
	v_cvt_pk_fp8_f32 v63, v30, v31 op_sel:[0,0,1]
	v_cvt_pk_fp8_f32 v64, v34, v35 op_sel:[0,0,1]
	v_cvt_pk_fp8_f32 v65, v38, v39 op_sel:[0,0,1]
	s_and_b32 s11, s4, 0x3fff
	s_lshl_b32 s11, s11, 7
	s_lshr_b32 s101, s4, 14
	s_lshl_b32 s101, s101, 25
	s_add_u32 s11, s11, s101
	v_add_u32_e32 v66, s11, v56
	v_add_u32_e32 v67, 0x400000, v66
	v_add_u32_e32 v68, 0x800000, v66
	v_add_u32_e32 v69, 0xc00000, v66
	v_add_u32_e32 v70, 0x1000000, v66
	v_add_u32_e32 v71, 0x1400000, v66
	v_add_u32_e32 v72, 0x1800000, v66
	v_add_u32_e32 v73, 0x1c00000, v66
	global_store_dword v66, v58, s[6:7] nt
	global_store_dword v67, v59, s[6:7] nt
	global_store_dword v68, v60, s[6:7] nt
	global_store_dword v69, v61, s[6:7] nt
	global_store_dword v70, v62, s[6:7] nt
	global_store_dword v71, v63, s[6:7] nt
	global_store_dword v72, v64, s[6:7] nt
	global_store_dword v73, v65, s[6:7] nt
	s_sleep 127
	s_add_u32 s4, s4, s10
	s_cmp_ge_u32 s4, 0x59d8
	s_cbranch_scc1 .Ldfb2_done
	s_add_u32 s11, s4, s10
	s_min_u32 s11, s11, 0x59d7
	s_mov_b32 s101, s11
	s_lshl_b32 s11, s101, 13
	v_add_u32_e32 v40, s11, v7
	v_add_u32_e32 v41, 0x1000, v40
	global_load_dwordx4 v[8:11], v40, s[8:9] nt
	global_load_dwordx4 v[12:15], v40, s[8:9] offset:1024 nt
	global_load_dwordx4 v[16:19], v40, s[8:9] offset:2048 nt
	global_load_dwordx4 v[20:23], v40, s[8:9] offset:3072 nt
	global_load_dwordx4 v[24:27], v41, s[8:9] nt
	global_load_dwordx4 v[28:31], v41, s[8:9] offset:1024 nt
	global_load_dwordx4 v[32:35], v41, s[8:9] offset:2048 nt
	global_load_dwordx4 v[36:39], v41, s[8:9] offset:3072 nt
	s_waitcnt vmcnt(8)
	v_max3_f32 v42, |v76|, |v77|, |v78|
	v_max3_f32 v43, |v80|, |v81|, |v82|
	v_max3_f32 v44, |v84|, |v85|, |v86|
	v_max3_f32 v45, |v88|, |v89|, |v90|
	v_max3_f32 v46, |v92|, |v93|, |v94|
	v_max3_f32 v47, |v96|, |v97|, |v98|
	v_max3_f32 v48, |v100|, |v101|, |v102|
	v_max3_f32 v49, |v104|, |v105|, |v106|
	v_max_f32_e64 v42, v42, |v79|
	v_max_f32_e64 v43, v43, |v83|
	v_max_f32_e64 v44, v44, |v87|
	v_max_f32_e64 v45, v45, |v91|
	v_max_f32_e64 v46, v46, |v95|
	v_max_f32_e64 v47, v47, |v99|
	v_max_f32_e64 v48, v48, |v103|
	v_max_f32_e64 v49, v49, |v107|
	v_max3_f32 v42, v42, v43, v44
	v_max3_f32 v45, v45, v46, v47
	v_max3_f32 v42, v42, v45, v48
	v_max_f32_e32 v42, v42, v49
	s_nop 1
	v_max_f32_dpp v43, v42, v42 quad_perm:[1,0,3,2] row_mask:0xf bank_mask:0xf bound_ctrl:1
	s_nop 1
	v_max_f32_dpp v42, v43, v43 quad_perm:[2,3,0,1] row_mask:0xf bank_mask:0xf bound_ctrl:1
	s_nop 1
	v_max_f32_dpp v43, v42, v42 row_half_mirror row_mask:0xf bank_mask:0xf bound_ctrl:1
	s_nop 1
	v_max_f32_dpp v42, v43, v43 row_mirror row_mask:0xf bank_mask:0xf bound_ctrl:1
	s_nop 1
	v_mov_b32_e32 v43, v42
	s_nop 1
	v_permlane16_swap_b32_e32 v42, v43
	v_max_f32_e32 v42, v42, v43
	v_mov_b32_e32 v43, v42
	s_nop 1
	v_permlane32_swap_b32_e32 v42, v43
	v_max_f32_e32 v49, v42, v43
	v_mul_f32_e32 v44, 0x3b124925, v49
	s_lshl_b32 s11, s4, 2
	s_add_u32 s11, s11, 0x12a20000
	v_mov_b32_e32 v45, s11
	s_mov_b64 exec, 1
	global_store_dword v45, v44, s[6:7]
	s_mov_b64 exec, -1
	v_mov_b32_e32 v46, 0x43e00000
	v_div_scale_f32 v42, s[100:101], v49, v49, v46
	v_rcp_f32_e32 v43, v42
	s_nop 0
	v_fma_f32 v44, -v42, v43, 1.0
	v_fmac_f32_e32 v43, v44, v43
	v_div_scale_f32 v44, vcc, v46, v49, v46
	v_mul_f32_e32 v45, v44, v43
	v_fma_f32 v47, -v42, v45, v44
	v_fmac_f32_e32 v45, v47, v43
	v_fma_f32 v42, -v42, v45, v44
	s_nop 1
	v_div_fmas_f32 v42, v42, v43, v45
	v_div_fixup_f32 v42, v42, v49, v46
	v_cmp_lt_f32_e32 vcc, 0, v49
	s_nop 1
	v_cndmask_b32_e32 v48, 0, v42, vcc
	v_mul_f32_e32 v76, v76, v48
	v_mul_f32_e32 v77, v77, v48
	v_mul_f32_e32 v78, v78, v48
	v_mul_f32_e32 v79, v79, v48
	v_mul_f32_e32 v80, v80, v48
	v_mul_f32_e32 v81, v81, v48
	v_mul_f32_e32 v82, v82, v48
	v_mul_f32_e32 v83, v83, v48
	v_mul_f32_e32 v84, v84, v48
	v_mul_f32_e32 v85, v85, v48
	v_mul_f32_e32 v86, v86, v48
	v_mul_f32_e32 v87, v87, v48
	v_mul_f32_e32 v88, v88, v48
	v_mul_f32_e32 v89, v89, v48
	v_mul_f32_e32 v90, v90, v48
	v_mul_f32_e32 v91, v91, v48
	v_mul_f32_e32 v92, v92, v48
	v_mul_f32_e32 v93, v93, v48
	v_mul_f32_e32 v94, v94, v48
	v_mul_f32_e32 v95, v95, v48
	v_mul_f32_e32 v96, v96, v48
	v_mul_f32_e32 v97, v97, v48
	v_mul_f32_e32 v98, v98, v48
	v_mul_f32_e32 v99, v99, v48
	v_mul_f32_e32 v100, v100, v48
	v_mul_f32_e32 v101, v101, v48
	v_mul_f32_e32 v102, v102, v48
	v_mul_f32_e32 v103, v103, v48
	v_mul_f32_e32 v104, v104, v48
	v_mul_f32_e32 v105, v105, v48
	v_mul_f32_e32 v106, v106, v48
	v_mul_f32_e32 v107, v107, v48
	v_mov_b32_e32 v58, 0
	v_mov_b32_e32 v59, 0
	v_mov_b32_e32 v60, 0
	v_mov_b32_e32 v61, 0
	v_mov_b32_e32 v62, 0
	v_mov_b32_e32 v63, 0
	v_mov_b32_e32 v64, 0
	v_mov_b32_e32 v65, 0
	v_cvt_pk_fp8_f32 v58, v76, v77
	v_cvt_pk_fp8_f32 v59, v80, v81
	v_cvt_pk_fp8_f32 v60, v84, v85
	v_cvt_pk_fp8_f32 v61, v88, v89
	v_cvt_pk_fp8_f32 v62, v92, v93
	v_cvt_pk_fp8_f32 v63, v96, v97
	v_cvt_pk_fp8_f32 v64, v100, v101
	v_cvt_pk_fp8_f32 v65, v104, v105
	v_cvt_pk_fp8_f32 v58, v78, v79 op_sel:[0,0,1]
	v_cvt_pk_fp8_f32 v59, v82, v83 op_sel:[0,0,1]
	v_cvt_pk_fp8_f32 v60, v86, v87 op_sel:[0,0,1]
	v_cvt_pk_fp8_f32 v61, v90, v91 op_sel:[0,0,1]
	v_cvt_pk_fp8_f32 v62, v94, v95 op_sel:[0,0,1]
	v_cvt_pk_fp8_f32 v63, v98, v99 op_sel:[0,0,1]
	v_cvt_pk_fp8_f32 v64, v102, v103 op_sel:[0,0,1]
	v_cvt_pk_fp8_f32 v65, v106, v107 op_sel:[0,0,1]
	s_and_b32 s11, s4, 0x3fff
	s_lshl_b32 s11, s11, 7
	s_lshr_b32 s101, s4, 14
	s_lshl_b32 s101, s101, 25
	s_add_u32 s11, s11, s101
	v_add_u32_e32 v66, s11, v56
	v_add_u32_e32 v67, 0x400000, v66
	v_add_u32_e32 v68, 0x800000, v66
	v_add_u32_e32 v69, 0xc00000, v66
	v_add_u32_e32 v70, 0x1000000, v66
	v_add_u32_e32 v71, 0x1400000, v66
	v_add_u32_e32 v72, 0x1800000, v66
	v_add_u32_e32 v73, 0x1c00000, v66
	global_store_dword v66, v58, s[6:7] nt
	global_store_dword v67, v59, s[6:7] nt
	global_store_dword v68, v60, s[6:7] nt
	global_store_dword v69, v61, s[6:7] nt
	global_store_dword v70, v62, s[6:7] nt
	global_store_dword v71, v63, s[6:7] nt
	global_store_dword v72, v64, s[6:7] nt
	global_store_dword v73, v65, s[6:7] nt
	s_sleep 127
	s_add_u32 s4, s4, s10
	s_cmp_ge_u32 s4, 0x59d8
	s_cbranch_scc1 .Ldfb2_done
	s_branch .Ldfb2_loop

.LBB0_856:
	v_readlane_b32 s4, v255, 36
	v_readlane_b32 s8, v252, 0
	s_add_i32 s5, s4, 10
	v_readlane_b32 s9, v252, 1
	s_cmp_ge_i32 s5, s9
	v_readlane_b32 s10, v252, 2
	v_readlane_b32 s11, v252, 3
	s_cbranch_scc1 .LBB0_906
	v_readlane_b32 s4, v255, 34
	s_nop 0
	s_cmp_lg_u32 s4, 0
	s_cbranch_scc1 .Ldfc_done
	s_cmp_gt_u32 s82, 32
	s_cselect_b32 s11, 32, 0
	s_cmp_lt_u32 s2, s11
	s_cbranch_scc1 .Ldfc_done
	s_sub_u32 s10, s82, s11
	s_lshl_b32 s10, s10, 3
	s_sub_u32 s4, s2, s11
	s_lshl_b32 s4, s4, 3
	v_readfirstlane_b32 s11, v0
	s_lshr_b32 s11, s11, 6
	s_add_u32 s4, s4, s11
	s_add_u32 s4, s4, 0x59d8
	s_cmp_ge_u32 s4, 0x8000
	s_cbranch_scc1 .Ldfc_done
	v_readlane_b32 s6, v252, 4
	v_readlane_b32 s7, v252, 5
	s_nop 0
	s_sub_u32 s6, s6, 0x38
	s_subb_u32 s7, s7, 0
	s_load_dwordx2 s[8:9], s[6:7], 0x8
	s_load_dwordx2 s[6:7], s[6:7], 0x20
	v_and_b32_e32 v6, 63, v0
	v_lshlrev_b32_e32 v7, 4, v6
	v_lshrrev_b32_e32 v56, 5, v6
	v_and_b32_e32 v57, 31, v6
	v_lshlrev_b32_e32 v56, 21, v56
	v_lshl_add_u32 v56, v57, 2, v56
	v_add_u32_e32 v56, 0xea00000, v56
	s_mov_b64 exec, -1
	s_waitcnt lgkmcnt(0)
	s_lshl_b32 s11, s4, 13
	v_add_u32_e32 v40, s11, v7
	v_add_u32_e32 v41, 0x1000, v40
	global_load_dwordx4 v[8:11], v40, s[8:9] nt
	global_load_dwordx4 v[12:15], v40, s[8:9] offset:1024 nt
	global_load_dwordx4 v[16:19], v40, s[8:9] offset:2048 nt
	global_load_dwordx4 v[20:23], v40, s[8:9] offset:3072 nt
	global_load_dwordx4 v[24:27], v41, s[8:9] nt
	global_load_dwordx4 v[28:31], v41, s[8:9] offset:1024 nt
	global_load_dwordx4 v[32:35], v41, s[8:9] offset:2048 nt
	global_load_dwordx4 v[36:39], v41, s[8:9] offset:3072 nt
.Ldfc_loop:
	s_add_u32 s11, s4, s10
	s_min_u32 s11, s11, 0x7fff
	s_mov_b32 s101, s11
	s_lshl_b32 s11, s101, 13
	v_add_u32_e32 v40, s11, v7
	v_add_u32_e32 v41, 0x1000, v40
	global_load_dwordx4 v[76:79], v40, s[8:9] nt
	global_load_dwordx4 v[80:83], v40, s[8:9] offset:1024 nt
	global_load_dwordx4 v[84:87], v40, s[8:9] offset:2048 nt
	global_load_dwordx4 v[88:91], v40, s[8:9] offset:3072 nt
	global_load_dwordx4 v[92:95], v41, s[8:9] nt
	global_load_dwordx4 v[96:99], v41, s[8:9] offset:1024 nt
	global_load_dwordx4 v[100:103], v41, s[8:9] offset:2048 nt
	global_load_dwordx4 v[104:107], v41, s[8:9] offset:3072 nt
	s_waitcnt vmcnt(8)
	v_max3_f32 v42, |v8|, |v9|, |v10|
	v_max3_f32 v43, |v12|, |v13|, |v14|
	v_max3_f32 v44, |v16|, |v17|, |v18|
	v_max3_f32 v45, |v20|, |v21|, |v22|
	v_max3_f32 v46, |v24|, |v25|, |v26|
	v_max3_f32 v47, |v28|, |v29|, |v30|
	v_max3_f32 v48, |v32|, |v33|, |v34|
	v_max3_f32 v49, |v36|, |v37|, |v38|
	v_max_f32_e64 v42, v42, |v11|
	v_max_f32_e64 v43, v43, |v15|
	v_max_f32_e64 v44, v44, |v19|
	v_max_f32_e64 v45, v45, |v23|
	v_max_f32_e64 v46, v46, |v27|
	v_max_f32_e64 v47, v47, |v31|
	v_max_f32_e64 v48, v48, |v35|
	v_max_f32_e64 v49, v49, |v39|
	v_max3_f32 v42, v42, v43, v44
	v_max3_f32 v45, v45, v46, v47
	v_max3_f32 v42, v42, v45, v48
	v_max_f32_e32 v42, v42, v49
	s_nop 1
	v_max_f32_dpp v43, v42, v42 quad_perm:[1,0,3,2] row_mask:0xf bank_mask:0xf bound_ctrl:1
	s_nop 1
	v_max_f32_dpp v42, v43, v43 quad_perm:[2,3,0,1] row_mask:0xf bank_mask:0xf bound_ctrl:1
	s_nop 1
	v_max_f32_dpp v43, v42, v42 row_half_mirror row_mask:0xf bank_mask:0xf bound_ctrl:1
	s_nop 1
	v_max_f32_dpp v42, v43, v43 row_mirror row_mask:0xf bank_mask:0xf bound_ctrl:1
	s_nop 1
	v_mov_b32_e32 v43, v42
	s_nop 1
	v_permlane16_swap_b32_e32 v42, v43
	v_max_f32_e32 v42, v42, v43
	v_mov_b32_e32 v43, v42
	s_nop 1
	v_permlane32_swap_b32_e32 v42, v43
	v_max_f32_e32 v49, v42, v43
	v_mul_f32_e32 v44, 0x3b124925, v49
	s_lshl_b32 s11, s4, 2
	s_add_u32 s11, s11, 0x12a20000
	v_mov_b32_e32 v45, s11
	s_mov_b64 exec, 1
	global_store_dword v45, v44, s[6:7]
	s_mov_b64 exec, -1
	v_mov_b32_e32 v46, 0x43e00000
	v_div_scale_f32 v42, s[100:101], v49, v49, v46
	v_rcp_f32_e32 v43, v42
	s_nop 0
	v_fma_f32 v44, -v42, v43, 1.0
	v_fmac_f32_e32 v43, v44, v43
	v_div_scale_f32 v44, vcc, v46, v49, v46
	v_mul_f32_e32 v45, v44, v43
	v_fma_f32 v47, -v42, v45, v44
	v_fmac_f32_e32 v45, v47, v43
	v_fma_f32 v42, -v42, v45, v44
	s_nop 1
	v_div_fmas_f32 v42, v42, v43, v45
	v_div_fixup_f32 v42, v42, v49, v46
	v_cmp_lt_f32_e32 vcc, 0, v49
	s_nop 1
	v_cndmask_b32_e32 v48, 0, v42, vcc
	v_mul_f32_e32 v8, v8, v48
	v_mul_f32_e32 v9, v9, v48
	v_mul_f32_e32 v10, v10, v48
	v_mul_f32_e32 v11, v11, v48
	v_mul_f32_e32 v12, v12, v48
	v_mul_f32_e32 v13, v13, v48
	v_mul_f32_e32 v14, v14, v48
	v_mul_f32_e32 v15, v15, v48
	v_mul_f32_e32 v16, v16, v48
	v_mul_f32_e32 v17, v17, v48
	v_mul_f32_e32 v18, v18, v48
	v_mul_f32_e32 v19, v19, v48
	v_mul_f32_e32 v20, v20, v48
	v_mul_f32_e32 v21, v21, v48
	v_mul_f32_e32 v22, v22, v48
	v_mul_f32_e32 v23, v23, v48
	v_mul_f32_e32 v24, v24, v48
	v_mul_f32_e32 v25, v25, v48
	v_mul_f32_e32 v26, v26, v48
	v_mul_f32_e32 v27, v27, v48
	v_mul_f32_e32 v28, v28, v48
	v_mul_f32_e32 v29, v29, v48
	v_mul_f32_e32 v30, v30, v48
	v_mul_f32_e32 v31, v31, v48
	v_mul_f32_e32 v32, v32, v48
	v_mul_f32_e32 v33, v33, v48
	v_mul_f32_e32 v34, v34, v48
	v_mul_f32_e32 v35, v35, v48
	v_mul_f32_e32 v36, v36, v48
	v_mul_f32_e32 v37, v37, v48
	v_mul_f32_e32 v38, v38, v48
	v_mul_f32_e32 v39, v39, v48
	v_mov_b32_e32 v58, 0
	v_mov_b32_e32 v59, 0
	v_mov_b32_e32 v60, 0
	v_mov_b32_e32 v61, 0
	v_mov_b32_e32 v62, 0
	v_mov_b32_e32 v63, 0
	v_mov_b32_e32 v64, 0
	v_mov_b32_e32 v65, 0
	v_cvt_pk_fp8_f32 v58, v8, v9
	v_cvt_pk_fp8_f32 v59, v12, v13
	v_cvt_pk_fp8_f32 v60, v16, v17
	v_cvt_pk_fp8_f32 v61, v20, v21
	v_cvt_pk_fp8_f32 v62, v24, v25
	v_cvt_pk_fp8_f32 v63, v28, v29
	v_cvt_pk_fp8_f32 v64, v32, v33
	v_cvt_pk_fp8_f32 v65, v36, v37
	v_cvt_pk_fp8_f32 v58, v10, v11 op_sel:[0,0,1]
	v_cvt_pk_fp8_f32 v59, v14, v15 op_sel:[0,0,1]
	v_cvt_pk_fp8_f32 v60, v18, v19 op_sel:[0,0,1]
	v_cvt_pk_fp8_f32 v61, v22, v23 op_sel:[0,0,1]
	v_cvt_pk_fp8_f32 v62, v26, v27 op_sel:[0,0,1]
	v_cvt_pk_fp8_f32 v63, v30, v31 op_sel:[0,0,1]
	v_cvt_pk_fp8_f32 v64, v34, v35 op_sel:[0,0,1]
	v_cvt_pk_fp8_f32 v65, v38, v39 op_sel:[0,0,1]
	s_and_b32 s11, s4, 0x3fff
	s_lshl_b32 s11, s11, 7
	s_lshr_b32 s101, s4, 14
	s_lshl_b32 s101, s101, 25
	s_add_u32 s11, s11, s101
	v_add_u32_e32 v66, s11, v56
	v_add_u32_e32 v67, 0x400000, v66
	v_add_u32_e32 v68, 0x800000, v66
	v_add_u32_e32 v69, 0xc00000, v66
	v_add_u32_e32 v70, 0x1000000, v66
	v_add_u32_e32 v71, 0x1400000, v66
	v_add_u32_e32 v72, 0x1800000, v66
	v_add_u32_e32 v73, 0x1c00000, v66
	global_store_dword v66, v58, s[6:7] nt
	global_store_dword v67, v59, s[6:7] nt
	global_store_dword v68, v60, s[6:7] nt
	global_store_dword v69, v61, s[6:7] nt
	global_store_dword v70, v62, s[6:7] nt
	global_store_dword v71, v63, s[6:7] nt
	global_store_dword v72, v64, s[6:7] nt
	global_store_dword v73, v65, s[6:7] nt
	s_sleep 127
	s_add_u32 s4, s4, s10
	s_cmp_ge_u32 s4, 0x8000
	s_cbranch_scc1 .Ldfc_done
	s_add_u32 s11, s4, s10
	s_min_u32 s11, s11, 0x7fff
	s_mov_b32 s101, s11
	s_lshl_b32 s11, s101, 13
	v_add_u32_e32 v40, s11, v7
	v_add_u32_e32 v41, 0x1000, v40
	global_load_dwordx4 v[8:11], v40, s[8:9] nt
	global_load_dwordx4 v[12:15], v40, s[8:9] offset:1024 nt
	global_load_dwordx4 v[16:19], v40, s[8:9] offset:2048 nt
	global_load_dwordx4 v[20:23], v40, s[8:9] offset:3072 nt
	global_load_dwordx4 v[24:27], v41, s[8:9] nt
	global_load_dwordx4 v[28:31], v41, s[8:9] offset:1024 nt
	global_load_dwordx4 v[32:35], v41, s[8:9] offset:2048 nt
	global_load_dwordx4 v[36:39], v41, s[8:9] offset:3072 nt
	s_waitcnt vmcnt(8)
	v_max3_f32 v42, |v76|, |v77|, |v78|
	v_max3_f32 v43, |v80|, |v81|, |v82|
	v_max3_f32 v44, |v84|, |v85|, |v86|
	v_max3_f32 v45, |v88|, |v89|, |v90|
	v_max3_f32 v46, |v92|, |v93|, |v94|
	v_max3_f32 v47, |v96|, |v97|, |v98|
	v_max3_f32 v48, |v100|, |v101|, |v102|
	v_max3_f32 v49, |v104|, |v105|, |v106|
	v_max_f32_e64 v42, v42, |v79|
	v_max_f32_e64 v43, v43, |v83|
	v_max_f32_e64 v44, v44, |v87|
	v_max_f32_e64 v45, v45, |v91|
	v_max_f32_e64 v46, v46, |v95|
	v_max_f32_e64 v47, v47, |v99|
	v_max_f32_e64 v48, v48, |v103|
	v_max_f32_e64 v49, v49, |v107|
	v_max3_f32 v42, v42, v43, v44
	v_max3_f32 v45, v45, v46, v47
	v_max3_f32 v42, v42, v45, v48
	v_max_f32_e32 v42, v42, v49
	s_nop 1
	v_max_f32_dpp v43, v42, v42 quad_perm:[1,0,3,2] row_mask:0xf bank_mask:0xf bound_ctrl:1
	s_nop 1
	v_max_f32_dpp v42, v43, v43 quad_perm:[2,3,0,1] row_mask:0xf bank_mask:0xf bound_ctrl:1
	s_nop 1
	v_max_f32_dpp v43, v42, v42 row_half_mirror row_mask:0xf bank_mask:0xf bound_ctrl:1
	s_nop 1
	v_max_f32_dpp v42, v43, v43 row_mirror row_mask:0xf bank_mask:0xf bound_ctrl:1
	s_nop 1
	v_mov_b32_e32 v43, v42
	s_nop 1
	v_permlane16_swap_b32_e32 v42, v43
	v_max_f32_e32 v42, v42, v43
	v_mov_b32_e32 v43, v42
	s_nop 1
	v_permlane32_swap_b32_e32 v42, v43
	v_max_f32_e32 v49, v42, v43
	v_mul_f32_e32 v44, 0x3b124925, v49
	s_lshl_b32 s11, s4, 2
	s_add_u32 s11, s11, 0x12a20000
	v_mov_b32_e32 v45, s11
	s_mov_b64 exec, 1
	global_store_dword v45, v44, s[6:7]
	s_mov_b64 exec, -1
	v_mov_b32_e32 v46, 0x43e00000
	v_div_scale_f32 v42, s[100:101], v49, v49, v46
	v_rcp_f32_e32 v43, v42
	s_nop 0
	v_fma_f32 v44, -v42, v43, 1.0
	v_fmac_f32_e32 v43, v44, v43
	v_div_scale_f32 v44, vcc, v46, v49, v46
	v_mul_f32_e32 v45, v44, v43
	v_fma_f32 v47, -v42, v45, v44
	v_fmac_f32_e32 v45, v47, v43
	v_fma_f32 v42, -v42, v45, v44
	s_nop 1
	v_div_fmas_f32 v42, v42, v43, v45
	v_div_fixup_f32 v42, v42, v49, v46
	v_cmp_lt_f32_e32 vcc, 0, v49
	s_nop 1
	v_cndmask_b32_e32 v48, 0, v42, vcc
	v_mul_f32_e32 v76, v76, v48
	v_mul_f32_e32 v77, v77, v48
	v_mul_f32_e32 v78, v78, v48
	v_mul_f32_e32 v79, v79, v48
	v_mul_f32_e32 v80, v80, v48
	v_mul_f32_e32 v81, v81, v48
	v_mul_f32_e32 v82, v82, v48
	v_mul_f32_e32 v83, v83, v48
	v_mul_f32_e32 v84, v84, v48
	v_mul_f32_e32 v85, v85, v48
	v_mul_f32_e32 v86, v86, v48
	v_mul_f32_e32 v87, v87, v48
	v_mul_f32_e32 v88, v88, v48
	v_mul_f32_e32 v89, v89, v48
	v_mul_f32_e32 v90, v90, v48
	v_mul_f32_e32 v91, v91, v48
	v_mul_f32_e32 v92, v92, v48
	v_mul_f32_e32 v93, v93, v48
	v_mul_f32_e32 v94, v94, v48
	v_mul_f32_e32 v95, v95, v48
	v_mul_f32_e32 v96, v96, v48
	v_mul_f32_e32 v97, v97, v48
	v_mul_f32_e32 v98, v98, v48
	v_mul_f32_e32 v99, v99, v48
	v_mul_f32_e32 v100, v100, v48
	v_mul_f32_e32 v101, v101, v48
	v_mul_f32_e32 v102, v102, v48
	v_mul_f32_e32 v103, v103, v48
	v_mul_f32_e32 v104, v104, v48
	v_mul_f32_e32 v105, v105, v48
	v_mul_f32_e32 v106, v106, v48
	v_mul_f32_e32 v107, v107, v48
	v_mov_b32_e32 v58, 0
	v_mov_b32_e32 v59, 0
	v_mov_b32_e32 v60, 0
	v_mov_b32_e32 v61, 0
	v_mov_b32_e32 v62, 0
	v_mov_b32_e32 v63, 0
	v_mov_b32_e32 v64, 0
	v_mov_b32_e32 v65, 0
	v_cvt_pk_fp8_f32 v58, v76, v77
	v_cvt_pk_fp8_f32 v59, v80, v81
	v_cvt_pk_fp8_f32 v60, v84, v85
	v_cvt_pk_fp8_f32 v61, v88, v89
	v_cvt_pk_fp8_f32 v62, v92, v93
	v_cvt_pk_fp8_f32 v63, v96, v97
	v_cvt_pk_fp8_f32 v64, v100, v101
	v_cvt_pk_fp8_f32 v65, v104, v105
	v_cvt_pk_fp8_f32 v58, v78, v79 op_sel:[0,0,1]
	v_cvt_pk_fp8_f32 v59, v82, v83 op_sel:[0,0,1]
	v_cvt_pk_fp8_f32 v60, v86, v87 op_sel:[0,0,1]
	v_cvt_pk_fp8_f32 v61, v90, v91 op_sel:[0,0,1]
	v_cvt_pk_fp8_f32 v62, v94, v95 op_sel:[0,0,1]
	v_cvt_pk_fp8_f32 v63, v98, v99 op_sel:[0,0,1]
	v_cvt_pk_fp8_f32 v64, v102, v103 op_sel:[0,0,1]
	v_cvt_pk_fp8_f32 v65, v106, v107 op_sel:[0,0,1]
	s_and_b32 s11, s4, 0x3fff
	s_lshl_b32 s11, s11, 7
	s_lshr_b32 s101, s4, 14
	s_lshl_b32 s101, s101, 25
	s_add_u32 s11, s11, s101
	v_add_u32_e32 v66, s11, v56
	v_add_u32_e32 v67, 0x400000, v66
	v_add_u32_e32 v68, 0x800000, v66
	v_add_u32_e32 v69, 0xc00000, v66
	v_add_u32_e32 v70, 0x1000000, v66
	v_add_u32_e32 v71, 0x1400000, v66
	v_add_u32_e32 v72, 0x1800000, v66
	v_add_u32_e32 v73, 0x1c00000, v66
	global_store_dword v66, v58, s[6:7] nt
	global_store_dword v67, v59, s[6:7] nt
	global_store_dword v68, v60, s[6:7] nt
	global_store_dword v69, v61, s[6:7] nt
	global_store_dword v70, v62, s[6:7] nt
	global_store_dword v71, v63, s[6:7] nt
	global_store_dword v72, v64, s[6:7] nt
	global_store_dword v73, v65, s[6:7] nt
	s_sleep 127
	s_add_u32 s4, s4, s10
	s_cmp_ge_u32 s4, 0x8000
	s_cbranch_scc1 .Ldfc_done
	s_branch .Ldfc_loop
